# attention micro-trims: redundant canonicalising max ops and fp8 dword zero-inits removed in epilogue and softmax head, on top of v27
# baseline (speedup 1.0000x reference)
.LBB0_809:
	s_nop 7
	v_max_f32_e32 v175, v82, v83


	v_max3_f32 v175, v175, v84, v85
	v_max3_f32 v175, v175, v86, v87
	v_max3_f32 v175, v175, v88, v89
	v_max3_f32 v175, v175, v90, v91
	v_max3_f32 v175, v175, v92, v93
	v_max3_f32 v175, v175, v94, v95
	v_max3_f32 v175, v175, v96, v97
	v_max3_f32 v175, v175, v66, v67
	v_max3_f32 v175, v175, v68, v69
	v_max3_f32 v175, v175, v70, v71
	v_max3_f32 v175, v175, v72, v73
	v_max3_f32 v175, v175, v74, v75
	v_max3_f32 v175, v175, v76, v77
	v_max3_f32 v175, v175, v78, v79
	v_max3_f32 v175, v175, v80, v81
	v_mov_b32_e32 v176, v175
	s_nop 1
	v_permlane32_swap_b32_e32 v175, v176


	v_max_f32_e32 v175, v175, v176
	v_cmp_ge_f32_e32 vcc, s76, v175
	s_cmp_eq_u64 vcc, exec
	s_cbranch_scc0 .Lsm1_slow
	v_mov_b32_e32 v222, 1.0

.LBB0_817:
	s_or_b64 exec, exec, s[56:57]
	v_and_b32_e32 v68, 64, v164
	v_xor_b32_e32 v67, 1, v164
	v_add_u32_e32 v68, 64, v68
	v_cmp_lt_i32_e32 vcc, v67, v68
	s_waitcnt lgkmcnt(0)
	s_lshl_b64 s[0:1], s[54:55], 11
	v_ashrrev_i32_e32 v73, 3, v167
	v_cndmask_b32_e32 v67, v164, v67, vcc
	v_lshlrev_b32_e32 v160, 2, v67
	v_xor_b32_e32 v67, 2, v164
	v_cmp_lt_i32_e32 vcc, v67, v68
	v_and_b32_e32 v66, -4, v73
	v_lshl_add_u32 v72, v66, 2, s65
	v_cndmask_b32_e32 v67, v164, v67, vcc
	v_lshlrev_b32_e32 v161, 2, v67
	v_and_b32_e32 v67, 3, v167
	v_cmp_eq_u32_e32 vcc, 0, v67
	ds_read_b32 v67, v72 offset:128
	s_add_u32 s0, s61, s0
	s_addc_u32 s1, s62, s1
	s_add_u32 s0, s0, s79
	v_and_b32_e32 v148, 31, v167
	s_waitcnt lgkmcnt(0)
	v_mul_f32_e32 v74, 0x41800000, v67
	v_mul_f32_e32 v75, v50, v74
	s_nop 1
	v_mov_b32_dpp v50, v75 quad_perm:[1,0,3,2] row_mask:0xf bank_mask:0xf
	s_nop 1
	v_mov_b32_dpp v77, v75 quad_perm:[2,3,0,1] row_mask:0xf bank_mask:0xf
	s_addc_u32 s1, s1, 0
	v_ashrrev_i32_e32 v67, 31, v66
	v_lshl_add_u64 v[68:69], s[0:1], 0, v[148:149]
	s_waitcnt lgkmcnt(0)
	s_nop 1
	v_mov_b32_dpp v76, v50 quad_perm:[2,3,0,1] row_mask:0xf bank_mask:0xf
	v_lshlrev_b64 v[70:71], 11, v[66:67]
	v_lshl_add_u64 v[70:71], v[68:69], 0, v[70:71]
	s_and_saveexec_b64 s[0:1], vcc
	s_cbranch_execz .LBB0_819


	v_med3_f32 v75, v75, s77, v166
	v_med3_f32 v50, v50, s77, v166

	v_cvt_pk_fp8_f32 v78, v75, v50
	v_max_f32_e32 v77, v77, v77
	s_waitcnt lgkmcnt(0)
	v_max_f32_e32 v75, v76, v76
	v_med3_f32 v50, v77, s77, v166
	v_med3_f32 v75, v75, s77, v166
	v_cvt_pk_fp8_f32 v78, v50, v75 op_sel:[0,0,1]
	global_store_dword v[70:71], v78, off
.LBB0_819:
	s_or_b64 exec, exec, s[0:1]
	s_waitcnt lgkmcnt(0)
	v_mul_f32_e32 v76, v34, v74
	s_nop 1
	v_mov_b32_dpp v75, v76 quad_perm:[1,0,3,2] row_mask:0xf bank_mask:0xf
	s_nop 1
	v_mov_b32_dpp v50, v76 quad_perm:[2,3,0,1] row_mask:0xf bank_mask:0xf
	s_waitcnt lgkmcnt(0)
	s_nop 1
	v_mov_b32_dpp v34, v75 quad_perm:[2,3,0,1] row_mask:0xf bank_mask:0xf
	s_and_saveexec_b64 s[0:1], vcc
	s_cbranch_execz .LBB0_821


	v_med3_f32 v76, v76, s77, v166
	v_med3_f32 v75, v75, s77, v166

	v_cvt_pk_fp8_f32 v77, v76, v75

	s_waitcnt lgkmcnt(0)

	v_med3_f32 v50, v50, s77, v166
	v_med3_f32 v34, v34, s77, v166
	v_cvt_pk_fp8_f32 v77, v50, v34 op_sel:[0,0,1]
	global_store_dword v[70:71], v77, off offset:32
.LBB0_821:
	s_or_b64 exec, exec, s[0:1]
	v_mul_f32_e32 v75, v18, v74
	s_nop 1
	v_mov_b32_dpp v50, v75 quad_perm:[1,0,3,2] row_mask:0xf bank_mask:0xf
	s_waitcnt lgkmcnt(0)
	s_nop 1
	v_mov_b32_dpp v34, v75 quad_perm:[2,3,0,1] row_mask:0xf bank_mask:0xf
	s_nop 1
	v_mov_b32_dpp v18, v50 quad_perm:[2,3,0,1] row_mask:0xf bank_mask:0xf
	s_and_saveexec_b64 s[0:1], vcc
	s_cbranch_execz .LBB0_823


	v_med3_f32 v75, v75, s77, v166
	v_med3_f32 v50, v50, s77, v166

	v_cvt_pk_fp8_f32 v76, v75, v50
	s_waitcnt lgkmcnt(0)


	v_med3_f32 v34, v34, s77, v166
	v_med3_f32 v18, v18, s77, v166
	v_cvt_pk_fp8_f32 v76, v34, v18 op_sel:[0,0,1]
	global_store_dword v[70:71], v76, off offset:64
.LBB0_823:
	s_or_b64 exec, exec, s[0:1]
	v_mul_f32_e32 v50, v2, v74
	s_waitcnt lgkmcnt(0)
	s_nop 1
	v_mov_b32_dpp v34, v50 quad_perm:[1,0,3,2] row_mask:0xf bank_mask:0xf
	s_nop 1
	v_mov_b32_dpp v18, v50 quad_perm:[2,3,0,1] row_mask:0xf bank_mask:0xf
	s_waitcnt lgkmcnt(0)
	s_nop 1
	v_mov_b32_dpp v2, v34 quad_perm:[2,3,0,1] row_mask:0xf bank_mask:0xf
	s_and_saveexec_b64 s[0:1], vcc
	s_cbranch_execz .LBB0_825


	v_med3_f32 v50, v50, s77, v166
	v_med3_f32 v34, v34, s77, v166

	v_cvt_pk_fp8_f32 v74, v50, v34

	s_waitcnt lgkmcnt(0)

	v_med3_f32 v18, v18, s77, v166
	v_med3_f32 v2, v2, s77, v166
	v_cvt_pk_fp8_f32 v74, v18, v2 op_sel:[0,0,1]
	global_store_dword v[70:71], v74, off offset:96
.LBB0_825:
	s_or_b64 exec, exec, s[0:1]
	s_waitcnt lgkmcnt(0)
	ds_read_b32 v2, v72 offset:132
	v_or_b32_e32 v70, 1, v66
	v_ashrrev_i32_e32 v71, 31, v70
	v_lshlrev_b64 v[70:71], 11, v[70:71]
	v_lshl_add_u64 v[70:71], v[68:69], 0, v[70:71]
	s_waitcnt lgkmcnt(0)
	v_mul_f32_e32 v2, 0x41800000, v2
	v_mul_f32_e32 v51, v51, v2
	s_nop 1
	v_mov_b32_dpp v50, v51 quad_perm:[1,0,3,2] row_mask:0xf bank_mask:0xf
	s_nop 1
	v_mov_b32_dpp v34, v51 quad_perm:[2,3,0,1] row_mask:0xf bank_mask:0xf
	s_waitcnt lgkmcnt(0)
	s_nop 1
	v_mov_b32_dpp v18, v50 quad_perm:[2,3,0,1] row_mask:0xf bank_mask:0xf
	s_and_saveexec_b64 s[0:1], vcc
	s_cbranch_execz .LBB0_827


	v_med3_f32 v51, v51, s77, v166
	v_med3_f32 v50, v50, s77, v166

	v_cvt_pk_fp8_f32 v74, v51, v50

	s_waitcnt lgkmcnt(0)

	v_med3_f32 v34, v34, s77, v166
	v_med3_f32 v18, v18, s77, v166
	v_cvt_pk_fp8_f32 v74, v34, v18 op_sel:[0,0,1]
	global_store_dword v[70:71], v74, off
.LBB0_827:
	s_or_b64 exec, exec, s[0:1]
	v_mul_f32_e32 v50, v35, v2
	s_nop 1
	v_mov_b32_dpp v35, v50 quad_perm:[1,0,3,2] row_mask:0xf bank_mask:0xf
	s_nop 1
	v_mov_b32_dpp v34, v50 quad_perm:[2,3,0,1] row_mask:0xf bank_mask:0xf
	s_waitcnt lgkmcnt(0)
	s_nop 1
	v_mov_b32_dpp v18, v35 quad_perm:[2,3,0,1] row_mask:0xf bank_mask:0xf
	s_and_saveexec_b64 s[0:1], vcc
	s_cbranch_execz .LBB0_829


	v_med3_f32 v50, v50, s77, v166
	v_med3_f32 v35, v35, s77, v166

	v_cvt_pk_fp8_f32 v51, v50, v35

	s_waitcnt lgkmcnt(0)

	v_med3_f32 v34, v34, s77, v166
	v_med3_f32 v18, v18, s77, v166
	v_cvt_pk_fp8_f32 v51, v34, v18 op_sel:[0,0,1]
	global_store_dword v[70:71], v51, off offset:32
.LBB0_829:
	s_or_b64 exec, exec, s[0:1]
	v_mul_f32_e32 v35, v19, v2
	s_nop 1
	v_mov_b32_dpp v34, v35 quad_perm:[1,0,3,2] row_mask:0xf bank_mask:0xf
	s_nop 1
	v_mov_b32_dpp v19, v35 quad_perm:[2,3,0,1] row_mask:0xf bank_mask:0xf
	s_waitcnt lgkmcnt(0)
	s_nop 1
	v_mov_b32_dpp v18, v34 quad_perm:[2,3,0,1] row_mask:0xf bank_mask:0xf
	s_and_saveexec_b64 s[0:1], vcc
	s_cbranch_execz .LBB0_831


	v_med3_f32 v35, v35, s77, v166
	v_med3_f32 v34, v34, s77, v166

	v_cvt_pk_fp8_f32 v50, v35, v34

	s_waitcnt lgkmcnt(0)

	v_med3_f32 v19, v19, s77, v166
	v_med3_f32 v18, v18, s77, v166
	v_cvt_pk_fp8_f32 v50, v19, v18 op_sel:[0,0,1]
	global_store_dword v[70:71], v50, off offset:64
.LBB0_831:
	s_or_b64 exec, exec, s[0:1]
	v_mul_f32_e32 v19, v3, v2
	s_waitcnt lgkmcnt(0)
	s_nop 1
	v_mov_b32_dpp v18, v19 quad_perm:[1,0,3,2] row_mask:0xf bank_mask:0xf
	s_nop 1
	v_mov_b32_dpp v3, v19 quad_perm:[2,3,0,1] row_mask:0xf bank_mask:0xf
	s_waitcnt lgkmcnt(0)
	s_nop 1
	v_mov_b32_dpp v2, v18 quad_perm:[2,3,0,1] row_mask:0xf bank_mask:0xf
	s_and_saveexec_b64 s[0:1], vcc
	s_cbranch_execz .LBB0_833


	v_med3_f32 v19, v19, s77, v166
	v_med3_f32 v18, v18, s77, v166

	v_cvt_pk_fp8_f32 v34, v19, v18

	s_waitcnt lgkmcnt(0)

	v_med3_f32 v3, v3, s77, v166
	v_med3_f32 v2, v2, s77, v166
	v_cvt_pk_fp8_f32 v34, v3, v2 op_sel:[0,0,1]
	global_store_dword v[70:71], v34, off offset:96
.LBB0_833:
	s_or_b64 exec, exec, s[0:1]
	ds_read_b32 v3, v72 offset:136
	s_waitcnt lgkmcnt(0)
	v_or_b32_e32 v2, 2, v66
	v_mul_f32_e32 v18, 0x41800000, v3
	v_mul_f32_e32 v50, v52, v18
	s_nop 1
	v_mov_b32_dpp v35, v50 quad_perm:[1,0,3,2] row_mask:0xf bank_mask:0xf
	s_nop 1
	v_mov_b32_dpp v34, v50 quad_perm:[2,3,0,1] row_mask:0xf bank_mask:0xf
	v_ashrrev_i32_e32 v3, 31, v2
	v_lshlrev_b64 v[2:3], 11, v[2:3]
	v_lshl_add_u64 v[2:3], v[68:69], 0, v[2:3]
	s_waitcnt lgkmcnt(0)
	s_nop 1
	v_mov_b32_dpp v19, v35 quad_perm:[2,3,0,1] row_mask:0xf bank_mask:0xf
	s_and_saveexec_b64 s[0:1], vcc
	s_cbranch_execz .LBB0_835


	v_med3_f32 v50, v50, s77, v166
	v_med3_f32 v35, v35, s77, v166

	v_cvt_pk_fp8_f32 v51, v50, v35

	s_waitcnt lgkmcnt(0)

	v_med3_f32 v34, v34, s77, v166
	v_med3_f32 v19, v19, s77, v166
	v_cvt_pk_fp8_f32 v51, v34, v19 op_sel:[0,0,1]
	global_store_dword v[2:3], v51, off
.LBB0_835:
	s_or_b64 exec, exec, s[0:1]
	v_mul_f32_e32 v36, v36, v18
	s_nop 1
	v_mov_b32_dpp v35, v36 quad_perm:[1,0,3,2] row_mask:0xf bank_mask:0xf
	s_nop 1
	v_mov_b32_dpp v34, v36 quad_perm:[2,3,0,1] row_mask:0xf bank_mask:0xf
	s_waitcnt lgkmcnt(0)
	s_nop 1
	v_mov_b32_dpp v19, v35 quad_perm:[2,3,0,1] row_mask:0xf bank_mask:0xf
	s_and_saveexec_b64 s[0:1], vcc
	s_cbranch_execz .LBB0_837


	v_med3_f32 v36, v36, s77, v166
	v_med3_f32 v35, v35, s77, v166

	v_cvt_pk_fp8_f32 v50, v36, v35

	s_waitcnt lgkmcnt(0)

	v_med3_f32 v34, v34, s77, v166
	v_med3_f32 v19, v19, s77, v166
	v_cvt_pk_fp8_f32 v50, v34, v19 op_sel:[0,0,1]
	global_store_dword v[2:3], v50, off offset:32
.LBB0_837:
	s_or_b64 exec, exec, s[0:1]
	v_mul_f32_e32 v35, v20, v18
	s_nop 1
	v_mov_b32_dpp v34, v35 quad_perm:[1,0,3,2] row_mask:0xf bank_mask:0xf
	s_nop 1
	v_mov_b32_dpp v20, v35 quad_perm:[2,3,0,1] row_mask:0xf bank_mask:0xf
	s_waitcnt lgkmcnt(0)
	s_nop 1
	v_mov_b32_dpp v19, v34 quad_perm:[2,3,0,1] row_mask:0xf bank_mask:0xf
	s_and_saveexec_b64 s[0:1], vcc
	s_cbranch_execz .LBB0_839


	v_med3_f32 v35, v35, s77, v166
	v_med3_f32 v34, v34, s77, v166

	v_cvt_pk_fp8_f32 v36, v35, v34

	s_waitcnt lgkmcnt(0)

	v_med3_f32 v20, v20, s77, v166
	v_med3_f32 v19, v19, s77, v166
	v_cvt_pk_fp8_f32 v36, v20, v19 op_sel:[0,0,1]
	global_store_dword v[2:3], v36, off offset:64
.LBB0_839:
	s_or_b64 exec, exec, s[0:1]
	v_mul_f32_e32 v20, v4, v18
	s_waitcnt lgkmcnt(0)
	s_nop 1
	v_mov_b32_dpp v19, v20 quad_perm:[1,0,3,2] row_mask:0xf bank_mask:0xf
	s_nop 1
	v_mov_b32_dpp v18, v20 quad_perm:[2,3,0,1] row_mask:0xf bank_mask:0xf
	s_waitcnt lgkmcnt(0)
	s_nop 1
	v_mov_b32_dpp v4, v19 quad_perm:[2,3,0,1] row_mask:0xf bank_mask:0xf
	s_and_saveexec_b64 s[0:1], vcc
	s_cbranch_execz .LBB0_841


	v_med3_f32 v20, v20, s77, v166
	v_med3_f32 v19, v19, s77, v166

	v_cvt_pk_fp8_f32 v34, v20, v19

	s_waitcnt lgkmcnt(0)

	v_med3_f32 v18, v18, s77, v166
	v_med3_f32 v4, v4, s77, v166
	v_cvt_pk_fp8_f32 v34, v18, v4 op_sel:[0,0,1]
	global_store_dword v[2:3], v34, off offset:96
.LBB0_841:
	s_or_b64 exec, exec, s[0:1]
	v_or_b32_e32 v2, 3, v73
	v_lshl_add_u32 v3, v2, 2, s65
	ds_read_b32 v3, v3 offset:128
	s_waitcnt lgkmcnt(0)
	v_mul_f32_e32 v4, 0x41800000, v3
	v_mul_f32_e32 v34, v53, v4
	s_nop 1
	v_mov_b32_dpp v20, v34 quad_perm:[1,0,3,2] row_mask:0xf bank_mask:0xf
	s_nop 1
	v_mov_b32_dpp v19, v34 quad_perm:[2,3,0,1] row_mask:0xf bank_mask:0xf
	v_ashrrev_i32_e32 v3, 31, v2
	v_lshlrev_b64 v[2:3], 11, v[2:3]
	v_lshl_add_u64 v[2:3], v[68:69], 0, v[2:3]
	s_waitcnt lgkmcnt(0)
	s_nop 1
	v_mov_b32_dpp v18, v20 quad_perm:[2,3,0,1] row_mask:0xf bank_mask:0xf
	s_and_saveexec_b64 s[0:1], vcc
	s_cbranch_execz .LBB0_843


	v_med3_f32 v34, v34, s77, v166
	v_med3_f32 v20, v20, s77, v166

	v_cvt_pk_fp8_f32 v35, v34, v20

	s_waitcnt lgkmcnt(0)

	v_med3_f32 v19, v19, s77, v166
	v_med3_f32 v18, v18, s77, v166
	v_cvt_pk_fp8_f32 v35, v19, v18 op_sel:[0,0,1]
	global_store_dword v[2:3], v35, off
.LBB0_843:
	s_or_b64 exec, exec, s[0:1]
	v_mul_f32_e32 v34, v37, v4
	s_nop 1
	v_mov_b32_dpp v20, v34 quad_perm:[1,0,3,2] row_mask:0xf bank_mask:0xf
	s_nop 1
	v_mov_b32_dpp v19, v34 quad_perm:[2,3,0,1] row_mask:0xf bank_mask:0xf
	s_waitcnt lgkmcnt(0)
	s_nop 1
	v_mov_b32_dpp v18, v20 quad_perm:[2,3,0,1] row_mask:0xf bank_mask:0xf
	s_and_saveexec_b64 s[0:1], vcc
	s_cbranch_execz .LBB0_845


	v_med3_f32 v34, v34, s77, v166
	v_med3_f32 v20, v20, s77, v166

	v_cvt_pk_fp8_f32 v35, v34, v20

	s_waitcnt lgkmcnt(0)

	v_med3_f32 v19, v19, s77, v166
	v_med3_f32 v18, v18, s77, v166
	v_cvt_pk_fp8_f32 v35, v19, v18 op_sel:[0,0,1]
	global_store_dword v[2:3], v35, off offset:32
.LBB0_845:
	s_or_b64 exec, exec, s[0:1]
	v_mul_f32_e32 v21, v21, v4
	s_nop 1
	v_mov_b32_dpp v20, v21 quad_perm:[1,0,3,2] row_mask:0xf bank_mask:0xf
	s_nop 1
	v_mov_b32_dpp v19, v21 quad_perm:[2,3,0,1] row_mask:0xf bank_mask:0xf
	s_waitcnt lgkmcnt(0)
	s_nop 1
	v_mov_b32_dpp v18, v20 quad_perm:[2,3,0,1] row_mask:0xf bank_mask:0xf
	s_and_saveexec_b64 s[0:1], vcc
	s_cbranch_execz .LBB0_847


	v_med3_f32 v21, v21, s77, v166
	v_med3_f32 v20, v20, s77, v166

	v_cvt_pk_fp8_f32 v34, v21, v20

	s_waitcnt lgkmcnt(0)

	v_med3_f32 v19, v19, s77, v166
	v_med3_f32 v18, v18, s77, v166
	v_cvt_pk_fp8_f32 v34, v19, v18 op_sel:[0,0,1]
	global_store_dword v[2:3], v34, off offset:64
.LBB0_847:
	s_or_b64 exec, exec, s[0:1]
	v_mul_f32_e32 v19, v5, v4
	s_waitcnt lgkmcnt(0)
	s_nop 1
	v_mov_b32_dpp v18, v19 quad_perm:[1,0,3,2] row_mask:0xf bank_mask:0xf
	s_nop 1
	v_mov_b32_dpp v5, v19 quad_perm:[2,3,0,1] row_mask:0xf bank_mask:0xf
	s_waitcnt lgkmcnt(0)
	s_nop 1
	v_mov_b32_dpp v4, v18 quad_perm:[2,3,0,1] row_mask:0xf bank_mask:0xf
	s_and_saveexec_b64 s[0:1], vcc
	s_cbranch_execz .LBB0_849


	v_med3_f32 v19, v19, s77, v166
	v_med3_f32 v18, v18, s77, v166

	v_cvt_pk_fp8_f32 v20, v19, v18

	s_waitcnt lgkmcnt(0)

	v_med3_f32 v5, v5, s77, v166
	v_med3_f32 v4, v4, s77, v166
	v_cvt_pk_fp8_f32 v20, v5, v4 op_sel:[0,0,1]
	global_store_dword v[2:3], v20, off offset:96
.LBB0_849:
	s_or_b64 exec, exec, s[0:1]
	ds_read_b32 v2, v72 offset:160
	s_waitcnt lgkmcnt(0)
	v_mul_f32_e32 v4, 0x41800000, v2
	v_mul_f32_e32 v20, v54, v4
	s_nop 1
	v_mov_b32_dpp v19, v20 quad_perm:[1,0,3,2] row_mask:0xf bank_mask:0xf
	s_nop 1
	v_mov_b32_dpp v18, v20 quad_perm:[2,3,0,1] row_mask:0xf bank_mask:0xf
	v_lshlrev_b64 v[2:3], 11, v[66:67]
	v_lshl_add_u64 v[2:3], v[68:69], 0, v[2:3]
	v_lshl_add_u64 v[2:3], v[2:3], 0, s[18:19]
	s_waitcnt lgkmcnt(0)
	s_nop 1
	v_mov_b32_dpp v5, v19 quad_perm:[2,3,0,1] row_mask:0xf bank_mask:0xf
	s_and_saveexec_b64 s[0:1], vcc
	s_cbranch_execz .LBB0_851


	v_med3_f32 v20, v20, s77, v166
	v_med3_f32 v19, v19, s77, v166

	v_cvt_pk_fp8_f32 v21, v20, v19

	s_waitcnt lgkmcnt(0)

	v_med3_f32 v18, v18, s77, v166
	v_med3_f32 v5, v5, s77, v166
	v_cvt_pk_fp8_f32 v21, v18, v5 op_sel:[0,0,1]
	global_store_dword v[2:3], v21, off
.LBB0_851:
	s_or_b64 exec, exec, s[0:1]
	v_mul_f32_e32 v20, v38, v4
	s_nop 1
	v_mov_b32_dpp v19, v20 quad_perm:[1,0,3,2] row_mask:0xf bank_mask:0xf
	s_nop 1
	v_mov_b32_dpp v18, v20 quad_perm:[2,3,0,1] row_mask:0xf bank_mask:0xf
	s_waitcnt lgkmcnt(0)
	s_nop 1
	v_mov_b32_dpp v5, v19 quad_perm:[2,3,0,1] row_mask:0xf bank_mask:0xf
	s_and_saveexec_b64 s[0:1], vcc
	s_cbranch_execz .LBB0_853


	v_med3_f32 v20, v20, s77, v166
	v_med3_f32 v19, v19, s77, v166

	v_cvt_pk_fp8_f32 v21, v20, v19

	s_waitcnt lgkmcnt(0)

	v_med3_f32 v18, v18, s77, v166
	v_med3_f32 v5, v5, s77, v166
	v_cvt_pk_fp8_f32 v21, v18, v5 op_sel:[0,0,1]
	global_store_dword v[2:3], v21, off offset:32
.LBB0_853:
	s_or_b64 exec, exec, s[0:1]
	v_mul_f32_e32 v20, v22, v4
	s_nop 1
	v_mov_b32_dpp v19, v20 quad_perm:[1,0,3,2] row_mask:0xf bank_mask:0xf
	s_nop 1
	v_mov_b32_dpp v18, v20 quad_perm:[2,3,0,1] row_mask:0xf bank_mask:0xf
	s_waitcnt lgkmcnt(0)
	s_nop 1
	v_mov_b32_dpp v5, v19 quad_perm:[2,3,0,1] row_mask:0xf bank_mask:0xf
	s_and_saveexec_b64 s[0:1], vcc
	s_cbranch_execz .LBB0_855


	v_med3_f32 v20, v20, s77, v166
	v_med3_f32 v19, v19, s77, v166

	v_cvt_pk_fp8_f32 v21, v20, v19

	s_waitcnt lgkmcnt(0)

	v_med3_f32 v18, v18, s77, v166
	v_med3_f32 v5, v5, s77, v166
	v_cvt_pk_fp8_f32 v21, v18, v5 op_sel:[0,0,1]
	global_store_dword v[2:3], v21, off offset:64
.LBB0_855:
	s_or_b64 exec, exec, s[0:1]
	v_mul_f32_e32 v18, v6, v4
	s_nop 1
	v_mov_b32_dpp v6, v18 quad_perm:[1,0,3,2] row_mask:0xf bank_mask:0xf
	s_waitcnt lgkmcnt(0)
	s_nop 1
	v_mov_b32_dpp v5, v18 quad_perm:[2,3,0,1] row_mask:0xf bank_mask:0xf
	s_nop 1
	v_mov_b32_dpp v4, v6 quad_perm:[2,3,0,1] row_mask:0xf bank_mask:0xf
	s_and_saveexec_b64 s[0:1], vcc
	s_cbranch_execz .LBB0_857


	v_med3_f32 v18, v18, s77, v166
	v_med3_f32 v6, v6, s77, v166

	v_cvt_pk_fp8_f32 v19, v18, v6
	s_waitcnt lgkmcnt(0)


	v_med3_f32 v5, v5, s77, v166
	v_med3_f32 v4, v4, s77, v166
	v_cvt_pk_fp8_f32 v19, v5, v4 op_sel:[0,0,1]
	global_store_dword v[2:3], v19, off offset:96
.LBB0_857:
	s_or_b64 exec, exec, s[0:1]
	ds_read_b32 v2, v72 offset:164
	s_waitcnt lgkmcnt(0)
	v_mul_f32_e32 v4, 0x41800000, v2
	v_mul_f32_e32 v19, v55, v4
	s_nop 1
	v_mov_b32_dpp v18, v19 quad_perm:[1,0,3,2] row_mask:0xf bank_mask:0xf
	s_nop 1
	v_mov_b32_dpp v6, v19 quad_perm:[2,3,0,1] row_mask:0xf bank_mask:0xf
	v_lshlrev_b64 v[2:3], 11, v[66:67]
	v_lshl_add_u64 v[2:3], v[68:69], 0, v[2:3]
	v_lshl_add_u64 v[2:3], v[2:3], 0, s[20:21]
	s_waitcnt lgkmcnt(0)
	s_nop 1
	v_mov_b32_dpp v5, v18 quad_perm:[2,3,0,1] row_mask:0xf bank_mask:0xf
	s_and_saveexec_b64 s[0:1], vcc
	s_cbranch_execz .LBB0_859


	v_med3_f32 v19, v19, s77, v166
	v_med3_f32 v18, v18, s77, v166

	v_cvt_pk_fp8_f32 v20, v19, v18

	s_waitcnt lgkmcnt(0)

	v_med3_f32 v6, v6, s77, v166
	v_med3_f32 v5, v5, s77, v166
	v_cvt_pk_fp8_f32 v20, v6, v5 op_sel:[0,0,1]
	global_store_dword v[2:3], v20, off
.LBB0_859:
	s_or_b64 exec, exec, s[0:1]
	v_mul_f32_e32 v19, v39, v4
	s_nop 1
	v_mov_b32_dpp v18, v19 quad_perm:[1,0,3,2] row_mask:0xf bank_mask:0xf
	s_nop 1
	v_mov_b32_dpp v6, v19 quad_perm:[2,3,0,1] row_mask:0xf bank_mask:0xf
	s_waitcnt lgkmcnt(0)
	s_nop 1
	v_mov_b32_dpp v5, v18 quad_perm:[2,3,0,1] row_mask:0xf bank_mask:0xf
	s_and_saveexec_b64 s[0:1], vcc
	s_cbranch_execz .LBB0_861


	v_med3_f32 v19, v19, s77, v166
	v_med3_f32 v18, v18, s77, v166

	v_cvt_pk_fp8_f32 v20, v19, v18

	s_waitcnt lgkmcnt(0)

	v_med3_f32 v6, v6, s77, v166
	v_med3_f32 v5, v5, s77, v166
	v_cvt_pk_fp8_f32 v20, v6, v5 op_sel:[0,0,1]
	global_store_dword v[2:3], v20, off offset:32
.LBB0_861:
	s_or_b64 exec, exec, s[0:1]
	v_mul_f32_e32 v19, v23, v4
	s_nop 1
	v_mov_b32_dpp v18, v19 quad_perm:[1,0,3,2] row_mask:0xf bank_mask:0xf
	s_nop 1
	v_mov_b32_dpp v6, v19 quad_perm:[2,3,0,1] row_mask:0xf bank_mask:0xf
	s_waitcnt lgkmcnt(0)
	s_nop 1
	v_mov_b32_dpp v5, v18 quad_perm:[2,3,0,1] row_mask:0xf bank_mask:0xf
	s_and_saveexec_b64 s[0:1], vcc
	s_cbranch_execz .LBB0_863


	v_med3_f32 v19, v19, s77, v166
	v_med3_f32 v18, v18, s77, v166

	v_cvt_pk_fp8_f32 v20, v19, v18

	s_waitcnt lgkmcnt(0)

	v_med3_f32 v6, v6, s77, v166
	v_med3_f32 v5, v5, s77, v166
	v_cvt_pk_fp8_f32 v20, v6, v5 op_sel:[0,0,1]
	global_store_dword v[2:3], v20, off offset:64
.LBB0_863:
	s_or_b64 exec, exec, s[0:1]
	v_mul_f32_e32 v7, v7, v4
	s_nop 1
	v_mov_b32_dpp v6, v7 quad_perm:[1,0,3,2] row_mask:0xf bank_mask:0xf
	s_waitcnt lgkmcnt(0)
	s_nop 1
	v_mov_b32_dpp v5, v7 quad_perm:[2,3,0,1] row_mask:0xf bank_mask:0xf
	s_nop 1
	v_mov_b32_dpp v4, v6 quad_perm:[2,3,0,1] row_mask:0xf bank_mask:0xf
	s_and_saveexec_b64 s[0:1], vcc
	s_cbranch_execz .LBB0_865


	v_med3_f32 v7, v7, s77, v166
	v_med3_f32 v6, v6, s77, v166

	v_cvt_pk_fp8_f32 v18, v7, v6
	s_waitcnt lgkmcnt(0)


	v_med3_f32 v5, v5, s77, v166
	v_med3_f32 v4, v4, s77, v166
	v_cvt_pk_fp8_f32 v18, v5, v4 op_sel:[0,0,1]
	global_store_dword v[2:3], v18, off offset:96
.LBB0_865:
	s_or_b64 exec, exec, s[0:1]
	ds_read_b32 v2, v72 offset:168
	s_waitcnt lgkmcnt(0)
	v_mul_f32_e32 v4, 0x41800000, v2
	v_mul_f32_e32 v18, v56, v4
	s_nop 1
	v_mov_b32_dpp v7, v18 quad_perm:[1,0,3,2] row_mask:0xf bank_mask:0xf
	s_nop 1
	v_mov_b32_dpp v6, v18 quad_perm:[2,3,0,1] row_mask:0xf bank_mask:0xf
	v_lshlrev_b64 v[2:3], 11, v[66:67]
	v_lshl_add_u64 v[2:3], v[68:69], 0, v[2:3]
	v_lshl_add_u64 v[2:3], v[2:3], 0, s[22:23]
	s_waitcnt lgkmcnt(0)
	s_nop 1
	v_mov_b32_dpp v5, v7 quad_perm:[2,3,0,1] row_mask:0xf bank_mask:0xf
	s_and_saveexec_b64 s[0:1], vcc
	s_cbranch_execz .LBB0_867


	v_med3_f32 v18, v18, s77, v166
	v_med3_f32 v7, v7, s77, v166

	v_cvt_pk_fp8_f32 v19, v18, v7

	s_waitcnt lgkmcnt(0)

	v_med3_f32 v6, v6, s77, v166
	v_med3_f32 v5, v5, s77, v166
	v_cvt_pk_fp8_f32 v19, v6, v5 op_sel:[0,0,1]
	global_store_dword v[2:3], v19, off
.LBB0_867:
	s_or_b64 exec, exec, s[0:1]
	v_mul_f32_e32 v18, v40, v4
	s_nop 1
	v_mov_b32_dpp v7, v18 quad_perm:[1,0,3,2] row_mask:0xf bank_mask:0xf
	s_nop 1
	v_mov_b32_dpp v6, v18 quad_perm:[2,3,0,1] row_mask:0xf bank_mask:0xf
	s_waitcnt lgkmcnt(0)
	s_nop 1
	v_mov_b32_dpp v5, v7 quad_perm:[2,3,0,1] row_mask:0xf bank_mask:0xf
	s_and_saveexec_b64 s[0:1], vcc
	s_cbranch_execz .LBB0_869


	v_med3_f32 v18, v18, s77, v166
	v_med3_f32 v7, v7, s77, v166

	v_cvt_pk_fp8_f32 v19, v18, v7

	s_waitcnt lgkmcnt(0)

	v_med3_f32 v6, v6, s77, v166
	v_med3_f32 v5, v5, s77, v166
	v_cvt_pk_fp8_f32 v19, v6, v5 op_sel:[0,0,1]
	global_store_dword v[2:3], v19, off offset:32
.LBB0_869:
	s_or_b64 exec, exec, s[0:1]
	v_mul_f32_e32 v18, v24, v4
	s_nop 1
	v_mov_b32_dpp v7, v18 quad_perm:[1,0,3,2] row_mask:0xf bank_mask:0xf
	s_nop 1
	v_mov_b32_dpp v6, v18 quad_perm:[2,3,0,1] row_mask:0xf bank_mask:0xf
	s_waitcnt lgkmcnt(0)
	s_nop 1
	v_mov_b32_dpp v5, v7 quad_perm:[2,3,0,1] row_mask:0xf bank_mask:0xf
	s_and_saveexec_b64 s[0:1], vcc
	s_cbranch_execz .LBB0_871


	v_med3_f32 v18, v18, s77, v166
	v_med3_f32 v7, v7, s77, v166

	v_cvt_pk_fp8_f32 v19, v18, v7

	s_waitcnt lgkmcnt(0)

	v_med3_f32 v6, v6, s77, v166
	v_med3_f32 v5, v5, s77, v166
	v_cvt_pk_fp8_f32 v19, v6, v5 op_sel:[0,0,1]
	global_store_dword v[2:3], v19, off offset:64
.LBB0_871:
	s_or_b64 exec, exec, s[0:1]
	v_mul_f32_e32 v7, v8, v4
	s_nop 1
	v_mov_b32_dpp v6, v7 quad_perm:[1,0,3,2] row_mask:0xf bank_mask:0xf
	s_waitcnt lgkmcnt(0)
	s_nop 1
	v_mov_b32_dpp v5, v7 quad_perm:[2,3,0,1] row_mask:0xf bank_mask:0xf
	s_nop 1
	v_mov_b32_dpp v4, v6 quad_perm:[2,3,0,1] row_mask:0xf bank_mask:0xf
	s_and_saveexec_b64 s[0:1], vcc
	s_cbranch_execz .LBB0_873


	v_med3_f32 v7, v7, s77, v166
	v_med3_f32 v6, v6, s77, v166

	v_cvt_pk_fp8_f32 v8, v7, v6
	s_waitcnt lgkmcnt(0)


	v_med3_f32 v5, v5, s77, v166
	v_med3_f32 v4, v4, s77, v166
	v_cvt_pk_fp8_f32 v8, v5, v4 op_sel:[0,0,1]
	global_store_dword v[2:3], v8, off offset:96
.LBB0_873:
	s_or_b64 exec, exec, s[0:1]
	ds_read_b32 v2, v72 offset:172
	s_waitcnt lgkmcnt(0)
	v_mul_f32_e32 v4, 0x41800000, v2
	v_mul_f32_e32 v8, v57, v4
	s_nop 1
	v_mov_b32_dpp v7, v8 quad_perm:[1,0,3,2] row_mask:0xf bank_mask:0xf
	s_nop 1
	v_mov_b32_dpp v6, v8 quad_perm:[2,3,0,1] row_mask:0xf bank_mask:0xf
	v_lshlrev_b64 v[2:3], 11, v[66:67]
	v_lshl_add_u64 v[2:3], v[68:69], 0, v[2:3]
	v_lshl_add_u64 v[2:3], v[2:3], 0, s[24:25]
	s_waitcnt lgkmcnt(0)
	s_nop 1
	v_mov_b32_dpp v5, v7 quad_perm:[2,3,0,1] row_mask:0xf bank_mask:0xf
	s_and_saveexec_b64 s[0:1], vcc
	s_cbranch_execz .LBB0_875


	v_med3_f32 v8, v8, s77, v166
	v_med3_f32 v7, v7, s77, v166

	v_cvt_pk_fp8_f32 v18, v8, v7

	s_waitcnt lgkmcnt(0)

	v_med3_f32 v6, v6, s77, v166
	v_med3_f32 v5, v5, s77, v166
	v_cvt_pk_fp8_f32 v18, v6, v5 op_sel:[0,0,1]
	global_store_dword v[2:3], v18, off
.LBB0_875:
	s_or_b64 exec, exec, s[0:1]
	v_mul_f32_e32 v8, v41, v4
	s_nop 1
	v_mov_b32_dpp v7, v8 quad_perm:[1,0,3,2] row_mask:0xf bank_mask:0xf
	s_nop 1
	v_mov_b32_dpp v6, v8 quad_perm:[2,3,0,1] row_mask:0xf bank_mask:0xf
	s_waitcnt lgkmcnt(0)
	s_nop 1
	v_mov_b32_dpp v5, v7 quad_perm:[2,3,0,1] row_mask:0xf bank_mask:0xf
	s_and_saveexec_b64 s[0:1], vcc
	s_cbranch_execz .LBB0_877


	v_med3_f32 v8, v8, s77, v166
	v_med3_f32 v7, v7, s77, v166

	v_cvt_pk_fp8_f32 v18, v8, v7

	s_waitcnt lgkmcnt(0)

	v_med3_f32 v6, v6, s77, v166
	v_med3_f32 v5, v5, s77, v166
	v_cvt_pk_fp8_f32 v18, v6, v5 op_sel:[0,0,1]
	global_store_dword v[2:3], v18, off offset:32
.LBB0_877:
	s_or_b64 exec, exec, s[0:1]
	v_mul_f32_e32 v8, v25, v4
	s_nop 1
	v_mov_b32_dpp v7, v8 quad_perm:[1,0,3,2] row_mask:0xf bank_mask:0xf
	s_nop 1
	v_mov_b32_dpp v6, v8 quad_perm:[2,3,0,1] row_mask:0xf bank_mask:0xf
	s_waitcnt lgkmcnt(0)
	s_nop 1
	v_mov_b32_dpp v5, v7 quad_perm:[2,3,0,1] row_mask:0xf bank_mask:0xf
	s_and_saveexec_b64 s[0:1], vcc
	s_cbranch_execz .LBB0_879


	v_med3_f32 v8, v8, s77, v166
	v_med3_f32 v7, v7, s77, v166

	v_cvt_pk_fp8_f32 v18, v8, v7

	s_waitcnt lgkmcnt(0)

	v_med3_f32 v6, v6, s77, v166
	v_med3_f32 v5, v5, s77, v166
	v_cvt_pk_fp8_f32 v18, v6, v5 op_sel:[0,0,1]
	global_store_dword v[2:3], v18, off offset:64
.LBB0_879:
	s_or_b64 exec, exec, s[0:1]
	v_mul_f32_e32 v7, v9, v4
	s_nop 1
	v_mov_b32_dpp v6, v7 quad_perm:[1,0,3,2] row_mask:0xf bank_mask:0xf
	s_waitcnt lgkmcnt(0)
	s_nop 1
	v_mov_b32_dpp v5, v7 quad_perm:[2,3,0,1] row_mask:0xf bank_mask:0xf
	s_nop 1
	v_mov_b32_dpp v4, v6 quad_perm:[2,3,0,1] row_mask:0xf bank_mask:0xf
	s_and_saveexec_b64 s[0:1], vcc
	s_cbranch_execz .LBB0_881


	v_med3_f32 v7, v7, s77, v166
	v_med3_f32 v6, v6, s77, v166

	v_cvt_pk_fp8_f32 v8, v7, v6
	s_waitcnt lgkmcnt(0)


	v_med3_f32 v5, v5, s77, v166
	v_med3_f32 v4, v4, s77, v166
	v_cvt_pk_fp8_f32 v8, v5, v4 op_sel:[0,0,1]
	global_store_dword v[2:3], v8, off offset:96
.LBB0_881:
	s_or_b64 exec, exec, s[0:1]
	ds_read_b32 v2, v72 offset:192
	s_waitcnt lgkmcnt(0)
	v_mul_f32_e32 v4, 0x41800000, v2
	v_mul_f32_e32 v8, v58, v4
	s_nop 1
	v_mov_b32_dpp v7, v8 quad_perm:[1,0,3,2] row_mask:0xf bank_mask:0xf
	s_nop 1
	v_mov_b32_dpp v6, v8 quad_perm:[2,3,0,1] row_mask:0xf bank_mask:0xf
	v_lshlrev_b64 v[2:3], 11, v[66:67]
	v_lshl_add_u64 v[2:3], v[68:69], 0, v[2:3]
	v_lshl_add_u64 v[2:3], v[2:3], 0, s[26:27]
	s_waitcnt lgkmcnt(0)
	s_nop 1
	v_mov_b32_dpp v5, v7 quad_perm:[2,3,0,1] row_mask:0xf bank_mask:0xf
	s_and_saveexec_b64 s[0:1], vcc
	s_cbranch_execz .LBB0_883


	v_med3_f32 v8, v8, s77, v166
	v_med3_f32 v7, v7, s77, v166

	v_cvt_pk_fp8_f32 v9, v8, v7

	s_waitcnt lgkmcnt(0)

	v_med3_f32 v6, v6, s77, v166
	v_med3_f32 v5, v5, s77, v166
	v_cvt_pk_fp8_f32 v9, v6, v5 op_sel:[0,0,1]
	global_store_dword v[2:3], v9, off
.LBB0_883:
	s_or_b64 exec, exec, s[0:1]
	v_mul_f32_e32 v8, v42, v4
	s_nop 1
	v_mov_b32_dpp v7, v8 quad_perm:[1,0,3,2] row_mask:0xf bank_mask:0xf
	s_nop 1
	v_mov_b32_dpp v6, v8 quad_perm:[2,3,0,1] row_mask:0xf bank_mask:0xf
	s_waitcnt lgkmcnt(0)
	s_nop 1
	v_mov_b32_dpp v5, v7 quad_perm:[2,3,0,1] row_mask:0xf bank_mask:0xf
	s_and_saveexec_b64 s[0:1], vcc
	s_cbranch_execz .LBB0_885


	v_med3_f32 v8, v8, s77, v166
	v_med3_f32 v7, v7, s77, v166

	v_cvt_pk_fp8_f32 v9, v8, v7

	s_waitcnt lgkmcnt(0)

	v_med3_f32 v6, v6, s77, v166
	v_med3_f32 v5, v5, s77, v166
	v_cvt_pk_fp8_f32 v9, v6, v5 op_sel:[0,0,1]
	global_store_dword v[2:3], v9, off offset:32
.LBB0_885:
	s_or_b64 exec, exec, s[0:1]
	v_mul_f32_e32 v8, v26, v4
	s_nop 1
	v_mov_b32_dpp v7, v8 quad_perm:[1,0,3,2] row_mask:0xf bank_mask:0xf
	s_nop 1
	v_mov_b32_dpp v6, v8 quad_perm:[2,3,0,1] row_mask:0xf bank_mask:0xf
	s_waitcnt lgkmcnt(0)
	s_nop 1
	v_mov_b32_dpp v5, v7 quad_perm:[2,3,0,1] row_mask:0xf bank_mask:0xf
	s_and_saveexec_b64 s[0:1], vcc
	s_cbranch_execz .LBB0_887


	v_med3_f32 v8, v8, s77, v166
	v_med3_f32 v7, v7, s77, v166

	v_cvt_pk_fp8_f32 v9, v8, v7

	s_waitcnt lgkmcnt(0)

	v_med3_f32 v6, v6, s77, v166
	v_med3_f32 v5, v5, s77, v166
	v_cvt_pk_fp8_f32 v9, v6, v5 op_sel:[0,0,1]
	global_store_dword v[2:3], v9, off offset:64
.LBB0_887:
	s_or_b64 exec, exec, s[0:1]
	v_mul_f32_e32 v7, v10, v4
	s_nop 1
	v_mov_b32_dpp v6, v7 quad_perm:[1,0,3,2] row_mask:0xf bank_mask:0xf
	s_waitcnt lgkmcnt(0)
	s_nop 1
	v_mov_b32_dpp v5, v7 quad_perm:[2,3,0,1] row_mask:0xf bank_mask:0xf
	s_nop 1
	v_mov_b32_dpp v4, v6 quad_perm:[2,3,0,1] row_mask:0xf bank_mask:0xf
	s_and_saveexec_b64 s[0:1], vcc
	s_cbranch_execz .LBB0_889


	v_med3_f32 v7, v7, s77, v166
	v_med3_f32 v6, v6, s77, v166

	v_cvt_pk_fp8_f32 v8, v7, v6
	s_waitcnt lgkmcnt(0)


	v_med3_f32 v5, v5, s77, v166
	v_med3_f32 v4, v4, s77, v166
	v_cvt_pk_fp8_f32 v8, v5, v4 op_sel:[0,0,1]
	global_store_dword v[2:3], v8, off offset:96
.LBB0_889:
	s_or_b64 exec, exec, s[0:1]
	ds_read_b32 v2, v72 offset:196
	s_waitcnt lgkmcnt(0)
	v_mul_f32_e32 v4, 0x41800000, v2
	v_mul_f32_e32 v8, v59, v4
	s_nop 1
	v_mov_b32_dpp v7, v8 quad_perm:[1,0,3,2] row_mask:0xf bank_mask:0xf
	s_nop 1
	v_mov_b32_dpp v6, v8 quad_perm:[2,3,0,1] row_mask:0xf bank_mask:0xf
	v_lshlrev_b64 v[2:3], 11, v[66:67]
	v_lshl_add_u64 v[2:3], v[68:69], 0, v[2:3]
	v_lshl_add_u64 v[2:3], v[2:3], 0, s[28:29]
	s_waitcnt lgkmcnt(0)
	s_nop 1
	v_mov_b32_dpp v5, v7 quad_perm:[2,3,0,1] row_mask:0xf bank_mask:0xf
	s_and_saveexec_b64 s[0:1], vcc
	s_cbranch_execz .LBB0_891


	v_med3_f32 v8, v8, s77, v166
	v_med3_f32 v7, v7, s77, v166

	v_cvt_pk_fp8_f32 v9, v8, v7

	s_waitcnt lgkmcnt(0)

	v_med3_f32 v6, v6, s77, v166
	v_med3_f32 v5, v5, s77, v166
	v_cvt_pk_fp8_f32 v9, v6, v5 op_sel:[0,0,1]
	global_store_dword v[2:3], v9, off
.LBB0_891:
	s_or_b64 exec, exec, s[0:1]
	v_mul_f32_e32 v8, v43, v4
	s_nop 1
	v_mov_b32_dpp v7, v8 quad_perm:[1,0,3,2] row_mask:0xf bank_mask:0xf
	s_nop 1
	v_mov_b32_dpp v6, v8 quad_perm:[2,3,0,1] row_mask:0xf bank_mask:0xf
	s_waitcnt lgkmcnt(0)
	s_nop 1
	v_mov_b32_dpp v5, v7 quad_perm:[2,3,0,1] row_mask:0xf bank_mask:0xf
	s_and_saveexec_b64 s[0:1], vcc
	s_cbranch_execz .LBB0_893


	v_med3_f32 v8, v8, s77, v166
	v_med3_f32 v7, v7, s77, v166

	v_cvt_pk_fp8_f32 v9, v8, v7

	s_waitcnt lgkmcnt(0)

	v_med3_f32 v6, v6, s77, v166
	v_med3_f32 v5, v5, s77, v166
	v_cvt_pk_fp8_f32 v9, v6, v5 op_sel:[0,0,1]
	global_store_dword v[2:3], v9, off offset:32
.LBB0_893:
	s_or_b64 exec, exec, s[0:1]
	v_mul_f32_e32 v8, v27, v4
	s_nop 1
	v_mov_b32_dpp v7, v8 quad_perm:[1,0,3,2] row_mask:0xf bank_mask:0xf
	s_nop 1
	v_mov_b32_dpp v6, v8 quad_perm:[2,3,0,1] row_mask:0xf bank_mask:0xf
	s_waitcnt lgkmcnt(0)
	s_nop 1
	v_mov_b32_dpp v5, v7 quad_perm:[2,3,0,1] row_mask:0xf bank_mask:0xf
	s_and_saveexec_b64 s[0:1], vcc
	s_cbranch_execz .LBB0_895


	v_med3_f32 v8, v8, s77, v166
	v_med3_f32 v7, v7, s77, v166

	v_cvt_pk_fp8_f32 v9, v8, v7

	s_waitcnt lgkmcnt(0)

	v_med3_f32 v6, v6, s77, v166
	v_med3_f32 v5, v5, s77, v166
	v_cvt_pk_fp8_f32 v9, v6, v5 op_sel:[0,0,1]
	global_store_dword v[2:3], v9, off offset:64
.LBB0_895:
	s_or_b64 exec, exec, s[0:1]
	v_mul_f32_e32 v7, v11, v4
	s_nop 1
	v_mov_b32_dpp v6, v7 quad_perm:[1,0,3,2] row_mask:0xf bank_mask:0xf
	s_waitcnt lgkmcnt(0)
	s_nop 1
	v_mov_b32_dpp v5, v7 quad_perm:[2,3,0,1] row_mask:0xf bank_mask:0xf
	s_nop 1
	v_mov_b32_dpp v4, v6 quad_perm:[2,3,0,1] row_mask:0xf bank_mask:0xf
	s_and_saveexec_b64 s[0:1], vcc
	s_cbranch_execz .LBB0_897


	v_med3_f32 v7, v7, s77, v166
	v_med3_f32 v6, v6, s77, v166

	v_cvt_pk_fp8_f32 v8, v7, v6
	s_waitcnt lgkmcnt(0)


	v_med3_f32 v5, v5, s77, v166
	v_med3_f32 v4, v4, s77, v166
	v_cvt_pk_fp8_f32 v8, v5, v4 op_sel:[0,0,1]
	global_store_dword v[2:3], v8, off offset:96
.LBB0_897:
	s_or_b64 exec, exec, s[0:1]
	ds_read_b32 v2, v72 offset:200
	s_waitcnt lgkmcnt(0)
	v_mul_f32_e32 v4, 0x41800000, v2
	v_mul_f32_e32 v8, v60, v4
	s_nop 1
	v_mov_b32_dpp v7, v8 quad_perm:[1,0,3,2] row_mask:0xf bank_mask:0xf
	s_nop 1
	v_mov_b32_dpp v6, v8 quad_perm:[2,3,0,1] row_mask:0xf bank_mask:0xf
	v_lshlrev_b64 v[2:3], 11, v[66:67]
	v_lshl_add_u64 v[2:3], v[68:69], 0, v[2:3]
	v_lshl_add_u64 v[2:3], v[2:3], 0, s[30:31]
	s_waitcnt lgkmcnt(0)
	s_nop 1
	v_mov_b32_dpp v5, v7 quad_perm:[2,3,0,1] row_mask:0xf bank_mask:0xf
	s_and_saveexec_b64 s[0:1], vcc
	s_cbranch_execz .LBB0_899


	v_med3_f32 v8, v8, s77, v166
	v_med3_f32 v7, v7, s77, v166

	v_cvt_pk_fp8_f32 v9, v8, v7

	s_waitcnt lgkmcnt(0)

	v_med3_f32 v6, v6, s77, v166
	v_med3_f32 v5, v5, s77, v166
	v_cvt_pk_fp8_f32 v9, v6, v5 op_sel:[0,0,1]
	global_store_dword v[2:3], v9, off
.LBB0_899:
	s_or_b64 exec, exec, s[0:1]
	v_mul_f32_e32 v8, v44, v4
	s_nop 1
	v_mov_b32_dpp v7, v8 quad_perm:[1,0,3,2] row_mask:0xf bank_mask:0xf
	s_nop 1
	v_mov_b32_dpp v6, v8 quad_perm:[2,3,0,1] row_mask:0xf bank_mask:0xf
	s_waitcnt lgkmcnt(0)
	s_nop 1
	v_mov_b32_dpp v5, v7 quad_perm:[2,3,0,1] row_mask:0xf bank_mask:0xf
	s_and_saveexec_b64 s[0:1], vcc
	s_cbranch_execz .LBB0_901


	v_med3_f32 v8, v8, s77, v166
	v_med3_f32 v7, v7, s77, v166

	v_cvt_pk_fp8_f32 v9, v8, v7

	s_waitcnt lgkmcnt(0)

	v_med3_f32 v6, v6, s77, v166
	v_med3_f32 v5, v5, s77, v166
	v_cvt_pk_fp8_f32 v9, v6, v5 op_sel:[0,0,1]
	global_store_dword v[2:3], v9, off offset:32
.LBB0_901:
	s_or_b64 exec, exec, s[0:1]
	v_mul_f32_e32 v8, v28, v4
	s_nop 1
	v_mov_b32_dpp v7, v8 quad_perm:[1,0,3,2] row_mask:0xf bank_mask:0xf
	s_nop 1
	v_mov_b32_dpp v6, v8 quad_perm:[2,3,0,1] row_mask:0xf bank_mask:0xf
	s_waitcnt lgkmcnt(0)
	s_nop 1
	v_mov_b32_dpp v5, v7 quad_perm:[2,3,0,1] row_mask:0xf bank_mask:0xf
	s_and_saveexec_b64 s[0:1], vcc
	s_cbranch_execz .LBB0_903


	v_med3_f32 v8, v8, s77, v166
	v_med3_f32 v7, v7, s77, v166

	v_cvt_pk_fp8_f32 v9, v8, v7

	s_waitcnt lgkmcnt(0)

	v_med3_f32 v6, v6, s77, v166
	v_med3_f32 v5, v5, s77, v166
	v_cvt_pk_fp8_f32 v9, v6, v5 op_sel:[0,0,1]
	global_store_dword v[2:3], v9, off offset:64
.LBB0_903:
	s_or_b64 exec, exec, s[0:1]
	v_mul_f32_e32 v7, v12, v4
	s_nop 1
	v_mov_b32_dpp v6, v7 quad_perm:[1,0,3,2] row_mask:0xf bank_mask:0xf
	s_waitcnt lgkmcnt(0)
	s_nop 1
	v_mov_b32_dpp v5, v7 quad_perm:[2,3,0,1] row_mask:0xf bank_mask:0xf
	s_nop 1
	v_mov_b32_dpp v4, v6 quad_perm:[2,3,0,1] row_mask:0xf bank_mask:0xf
	s_and_saveexec_b64 s[0:1], vcc
	s_cbranch_execz .LBB0_905


	v_med3_f32 v7, v7, s77, v166
	v_med3_f32 v6, v6, s77, v166

	v_cvt_pk_fp8_f32 v8, v7, v6
	s_waitcnt lgkmcnt(0)


	v_med3_f32 v5, v5, s77, v166
	v_med3_f32 v4, v4, s77, v166
	v_cvt_pk_fp8_f32 v8, v5, v4 op_sel:[0,0,1]
	global_store_dword v[2:3], v8, off offset:96
.LBB0_905:
	s_or_b64 exec, exec, s[0:1]
	ds_read_b32 v2, v72 offset:204
	s_waitcnt lgkmcnt(0)
	v_mul_f32_e32 v4, 0x41800000, v2
	v_mul_f32_e32 v8, v61, v4
	s_nop 1
	v_mov_b32_dpp v7, v8 quad_perm:[1,0,3,2] row_mask:0xf bank_mask:0xf
	s_nop 1
	v_mov_b32_dpp v6, v8 quad_perm:[2,3,0,1] row_mask:0xf bank_mask:0xf
	v_lshlrev_b64 v[2:3], 11, v[66:67]
	v_lshl_add_u64 v[2:3], v[68:69], 0, v[2:3]
	v_lshl_add_u64 v[2:3], v[2:3], 0, s[34:35]
	s_waitcnt lgkmcnt(0)
	s_nop 1
	v_mov_b32_dpp v5, v7 quad_perm:[2,3,0,1] row_mask:0xf bank_mask:0xf
	s_and_saveexec_b64 s[0:1], vcc
	s_cbranch_execz .LBB0_907


	v_med3_f32 v8, v8, s77, v166
	v_med3_f32 v7, v7, s77, v166

	v_cvt_pk_fp8_f32 v9, v8, v7

	s_waitcnt lgkmcnt(0)

	v_med3_f32 v6, v6, s77, v166
	v_med3_f32 v5, v5, s77, v166
	v_cvt_pk_fp8_f32 v9, v6, v5 op_sel:[0,0,1]
	global_store_dword v[2:3], v9, off
.LBB0_907:
	s_or_b64 exec, exec, s[0:1]
	v_mul_f32_e32 v8, v45, v4
	s_nop 1
	v_mov_b32_dpp v7, v8 quad_perm:[1,0,3,2] row_mask:0xf bank_mask:0xf
	s_nop 1
	v_mov_b32_dpp v6, v8 quad_perm:[2,3,0,1] row_mask:0xf bank_mask:0xf
	s_waitcnt lgkmcnt(0)
	s_nop 1
	v_mov_b32_dpp v5, v7 quad_perm:[2,3,0,1] row_mask:0xf bank_mask:0xf
	s_and_saveexec_b64 s[0:1], vcc
	s_cbranch_execz .LBB0_909


	v_med3_f32 v8, v8, s77, v166
	v_med3_f32 v7, v7, s77, v166

	v_cvt_pk_fp8_f32 v9, v8, v7

	s_waitcnt lgkmcnt(0)

	v_med3_f32 v6, v6, s77, v166
	v_med3_f32 v5, v5, s77, v166
	v_cvt_pk_fp8_f32 v9, v6, v5 op_sel:[0,0,1]
	global_store_dword v[2:3], v9, off offset:32
.LBB0_909:
	s_or_b64 exec, exec, s[0:1]
	v_mul_f32_e32 v8, v29, v4
	s_nop 1
	v_mov_b32_dpp v7, v8 quad_perm:[1,0,3,2] row_mask:0xf bank_mask:0xf
	s_nop 1
	v_mov_b32_dpp v6, v8 quad_perm:[2,3,0,1] row_mask:0xf bank_mask:0xf
	s_waitcnt lgkmcnt(0)
	s_nop 1
	v_mov_b32_dpp v5, v7 quad_perm:[2,3,0,1] row_mask:0xf bank_mask:0xf
	s_and_saveexec_b64 s[0:1], vcc
	s_cbranch_execz .LBB0_911


	v_med3_f32 v8, v8, s77, v166
	v_med3_f32 v7, v7, s77, v166

	v_cvt_pk_fp8_f32 v9, v8, v7

	s_waitcnt lgkmcnt(0)

	v_med3_f32 v6, v6, s77, v166
	v_med3_f32 v5, v5, s77, v166
	v_cvt_pk_fp8_f32 v9, v6, v5 op_sel:[0,0,1]
	global_store_dword v[2:3], v9, off offset:64
.LBB0_911:
	s_or_b64 exec, exec, s[0:1]
	v_mul_f32_e32 v7, v13, v4
	s_nop 1
	v_mov_b32_dpp v6, v7 quad_perm:[1,0,3,2] row_mask:0xf bank_mask:0xf
	s_waitcnt lgkmcnt(0)
	s_nop 1
	v_mov_b32_dpp v5, v7 quad_perm:[2,3,0,1] row_mask:0xf bank_mask:0xf
	s_nop 1
	v_mov_b32_dpp v4, v6 quad_perm:[2,3,0,1] row_mask:0xf bank_mask:0xf
	s_and_saveexec_b64 s[0:1], vcc
	s_cbranch_execz .LBB0_913


	v_med3_f32 v7, v7, s77, v166
	v_med3_f32 v6, v6, s77, v166

	v_cvt_pk_fp8_f32 v8, v7, v6
	s_waitcnt lgkmcnt(0)


	v_med3_f32 v5, v5, s77, v166
	v_med3_f32 v4, v4, s77, v166
	v_cvt_pk_fp8_f32 v8, v5, v4 op_sel:[0,0,1]
	global_store_dword v[2:3], v8, off offset:96
.LBB0_913:
	s_or_b64 exec, exec, s[0:1]
	ds_read_b32 v2, v72 offset:224
	s_waitcnt lgkmcnt(0)
	v_mul_f32_e32 v4, 0x41800000, v2
	v_mul_f32_e32 v8, v62, v4
	s_nop 1
	v_mov_b32_dpp v7, v8 quad_perm:[1,0,3,2] row_mask:0xf bank_mask:0xf
	s_nop 1
	v_mov_b32_dpp v6, v8 quad_perm:[2,3,0,1] row_mask:0xf bank_mask:0xf
	v_lshlrev_b64 v[2:3], 11, v[66:67]
	v_lshl_add_u64 v[2:3], v[68:69], 0, v[2:3]
	v_lshl_add_u64 v[2:3], v[2:3], 0, s[36:37]
	s_waitcnt lgkmcnt(0)
	s_nop 1
	v_mov_b32_dpp v5, v7 quad_perm:[2,3,0,1] row_mask:0xf bank_mask:0xf
	s_and_saveexec_b64 s[0:1], vcc
	s_cbranch_execz .LBB0_915


	v_med3_f32 v8, v8, s77, v166
	v_med3_f32 v7, v7, s77, v166

	v_cvt_pk_fp8_f32 v9, v8, v7

	s_waitcnt lgkmcnt(0)

	v_med3_f32 v6, v6, s77, v166
	v_med3_f32 v5, v5, s77, v166
	v_cvt_pk_fp8_f32 v9, v6, v5 op_sel:[0,0,1]
	global_store_dword v[2:3], v9, off
.LBB0_915:
	s_or_b64 exec, exec, s[0:1]
	v_mul_f32_e32 v8, v46, v4
	s_nop 1
	v_mov_b32_dpp v7, v8 quad_perm:[1,0,3,2] row_mask:0xf bank_mask:0xf
	s_nop 1
	v_mov_b32_dpp v6, v8 quad_perm:[2,3,0,1] row_mask:0xf bank_mask:0xf
	s_waitcnt lgkmcnt(0)
	s_nop 1
	v_mov_b32_dpp v5, v7 quad_perm:[2,3,0,1] row_mask:0xf bank_mask:0xf
	s_and_saveexec_b64 s[0:1], vcc
	s_cbranch_execz .LBB0_917


	v_med3_f32 v8, v8, s77, v166
	v_med3_f32 v7, v7, s77, v166

	v_cvt_pk_fp8_f32 v9, v8, v7

	s_waitcnt lgkmcnt(0)

	v_med3_f32 v6, v6, s77, v166
	v_med3_f32 v5, v5, s77, v166
	v_cvt_pk_fp8_f32 v9, v6, v5 op_sel:[0,0,1]
	global_store_dword v[2:3], v9, off offset:32
.LBB0_917:
	s_or_b64 exec, exec, s[0:1]
	v_mul_f32_e32 v8, v30, v4
	s_nop 1
	v_mov_b32_dpp v7, v8 quad_perm:[1,0,3,2] row_mask:0xf bank_mask:0xf
	s_nop 1
	v_mov_b32_dpp v6, v8 quad_perm:[2,3,0,1] row_mask:0xf bank_mask:0xf
	s_waitcnt lgkmcnt(0)
	s_nop 1
	v_mov_b32_dpp v5, v7 quad_perm:[2,3,0,1] row_mask:0xf bank_mask:0xf
	s_and_saveexec_b64 s[0:1], vcc
	s_cbranch_execz .LBB0_919


	v_med3_f32 v8, v8, s77, v166
	v_med3_f32 v7, v7, s77, v166

	v_cvt_pk_fp8_f32 v9, v8, v7

	s_waitcnt lgkmcnt(0)

	v_med3_f32 v6, v6, s77, v166
	v_med3_f32 v5, v5, s77, v166
	v_cvt_pk_fp8_f32 v9, v6, v5 op_sel:[0,0,1]
	global_store_dword v[2:3], v9, off offset:64
.LBB0_919:
	s_or_b64 exec, exec, s[0:1]
	v_mul_f32_e32 v7, v14, v4
	s_nop 1
	v_mov_b32_dpp v6, v7 quad_perm:[1,0,3,2] row_mask:0xf bank_mask:0xf
	s_waitcnt lgkmcnt(0)
	s_nop 1
	v_mov_b32_dpp v5, v7 quad_perm:[2,3,0,1] row_mask:0xf bank_mask:0xf
	s_nop 1
	v_mov_b32_dpp v4, v6 quad_perm:[2,3,0,1] row_mask:0xf bank_mask:0xf
	s_and_saveexec_b64 s[0:1], vcc
	s_cbranch_execz .LBB0_921


	v_med3_f32 v7, v7, s77, v166
	v_med3_f32 v6, v6, s77, v166

	v_cvt_pk_fp8_f32 v8, v7, v6
	s_waitcnt lgkmcnt(0)


	v_med3_f32 v5, v5, s77, v166
	v_med3_f32 v4, v4, s77, v166
	v_cvt_pk_fp8_f32 v8, v5, v4 op_sel:[0,0,1]
	global_store_dword v[2:3], v8, off offset:96
.LBB0_921:
	s_or_b64 exec, exec, s[0:1]
	ds_read_b32 v2, v72 offset:228
	s_waitcnt lgkmcnt(0)
	v_mul_f32_e32 v4, 0x41800000, v2
	v_mul_f32_e32 v8, v63, v4
	s_nop 1
	v_mov_b32_dpp v7, v8 quad_perm:[1,0,3,2] row_mask:0xf bank_mask:0xf
	s_nop 1
	v_mov_b32_dpp v6, v8 quad_perm:[2,3,0,1] row_mask:0xf bank_mask:0xf
	v_lshlrev_b64 v[2:3], 11, v[66:67]
	v_lshl_add_u64 v[2:3], v[68:69], 0, v[2:3]
	v_lshl_add_u64 v[2:3], v[2:3], 0, s[38:39]
	s_waitcnt lgkmcnt(0)
	s_nop 1
	v_mov_b32_dpp v5, v7 quad_perm:[2,3,0,1] row_mask:0xf bank_mask:0xf
	s_and_saveexec_b64 s[0:1], vcc
	s_cbranch_execz .LBB0_923


	v_med3_f32 v8, v8, s77, v166
	v_med3_f32 v7, v7, s77, v166

	v_cvt_pk_fp8_f32 v9, v8, v7

	s_waitcnt lgkmcnt(0)

	v_med3_f32 v6, v6, s77, v166
	v_med3_f32 v5, v5, s77, v166
	v_cvt_pk_fp8_f32 v9, v6, v5 op_sel:[0,0,1]
	global_store_dword v[2:3], v9, off
.LBB0_923:
	s_or_b64 exec, exec, s[0:1]
	v_mul_f32_e32 v8, v47, v4
	s_nop 1
	v_mov_b32_dpp v7, v8 quad_perm:[1,0,3,2] row_mask:0xf bank_mask:0xf
	s_nop 1
	v_mov_b32_dpp v6, v8 quad_perm:[2,3,0,1] row_mask:0xf bank_mask:0xf
	s_waitcnt lgkmcnt(0)
	s_nop 1
	v_mov_b32_dpp v5, v7 quad_perm:[2,3,0,1] row_mask:0xf bank_mask:0xf
	s_and_saveexec_b64 s[0:1], vcc
	s_cbranch_execz .LBB0_925


	v_med3_f32 v8, v8, s77, v166
	v_med3_f32 v7, v7, s77, v166

	v_cvt_pk_fp8_f32 v9, v8, v7

	s_waitcnt lgkmcnt(0)

	v_med3_f32 v6, v6, s77, v166
	v_med3_f32 v5, v5, s77, v166
	v_cvt_pk_fp8_f32 v9, v6, v5 op_sel:[0,0,1]
	global_store_dword v[2:3], v9, off offset:32
.LBB0_925:
	s_or_b64 exec, exec, s[0:1]
	v_mul_f32_e32 v8, v31, v4
	s_nop 1
	v_mov_b32_dpp v7, v8 quad_perm:[1,0,3,2] row_mask:0xf bank_mask:0xf
	s_nop 1
	v_mov_b32_dpp v6, v8 quad_perm:[2,3,0,1] row_mask:0xf bank_mask:0xf
	s_waitcnt lgkmcnt(0)
	s_nop 1
	v_mov_b32_dpp v5, v7 quad_perm:[2,3,0,1] row_mask:0xf bank_mask:0xf
	s_and_saveexec_b64 s[0:1], vcc
	s_cbranch_execz .LBB0_927


	v_med3_f32 v8, v8, s77, v166
	v_med3_f32 v7, v7, s77, v166

	v_cvt_pk_fp8_f32 v9, v8, v7

	s_waitcnt lgkmcnt(0)

	v_med3_f32 v6, v6, s77, v166
	v_med3_f32 v5, v5, s77, v166
	v_cvt_pk_fp8_f32 v9, v6, v5 op_sel:[0,0,1]
	global_store_dword v[2:3], v9, off offset:64
.LBB0_927:
	s_or_b64 exec, exec, s[0:1]
	v_mul_f32_e32 v7, v15, v4
	s_nop 1
	v_mov_b32_dpp v6, v7 quad_perm:[1,0,3,2] row_mask:0xf bank_mask:0xf
	s_waitcnt lgkmcnt(0)
	s_nop 1
	v_mov_b32_dpp v5, v7 quad_perm:[2,3,0,1] row_mask:0xf bank_mask:0xf
	s_nop 1
	v_mov_b32_dpp v4, v6 quad_perm:[2,3,0,1] row_mask:0xf bank_mask:0xf
	s_and_saveexec_b64 s[0:1], vcc
	s_cbranch_execz .LBB0_929


	v_med3_f32 v7, v7, s77, v166
	v_med3_f32 v6, v6, s77, v166

	v_cvt_pk_fp8_f32 v8, v7, v6
	s_waitcnt lgkmcnt(0)


	v_med3_f32 v5, v5, s77, v166
	v_med3_f32 v4, v4, s77, v166
	v_cvt_pk_fp8_f32 v8, v5, v4 op_sel:[0,0,1]
	global_store_dword v[2:3], v8, off offset:96
.LBB0_929:
	s_or_b64 exec, exec, s[0:1]
	ds_read_b32 v2, v72 offset:232
	s_waitcnt lgkmcnt(0)
	v_mul_f32_e32 v4, 0x41800000, v2
	v_mul_f32_e32 v8, v64, v4
	s_nop 1
	v_mov_b32_dpp v7, v8 quad_perm:[1,0,3,2] row_mask:0xf bank_mask:0xf
	s_nop 1
	v_mov_b32_dpp v6, v8 quad_perm:[2,3,0,1] row_mask:0xf bank_mask:0xf
	v_lshlrev_b64 v[2:3], 11, v[66:67]
	v_lshl_add_u64 v[2:3], v[68:69], 0, v[2:3]
	v_lshl_add_u64 v[2:3], v[2:3], 0, s[40:41]
	s_waitcnt lgkmcnt(0)
	s_nop 1
	v_mov_b32_dpp v5, v7 quad_perm:[2,3,0,1] row_mask:0xf bank_mask:0xf
	s_and_saveexec_b64 s[0:1], vcc
	s_cbranch_execz .LBB0_931


	v_med3_f32 v8, v8, s77, v166
	v_med3_f32 v7, v7, s77, v166

	v_cvt_pk_fp8_f32 v9, v8, v7

	s_waitcnt lgkmcnt(0)

	v_med3_f32 v6, v6, s77, v166
	v_med3_f32 v5, v5, s77, v166
	v_cvt_pk_fp8_f32 v9, v6, v5 op_sel:[0,0,1]
	global_store_dword v[2:3], v9, off
.LBB0_931:
	s_or_b64 exec, exec, s[0:1]
	v_mul_f32_e32 v8, v48, v4
	s_nop 1
	v_mov_b32_dpp v7, v8 quad_perm:[1,0,3,2] row_mask:0xf bank_mask:0xf
	s_nop 1
	v_mov_b32_dpp v6, v8 quad_perm:[2,3,0,1] row_mask:0xf bank_mask:0xf
	s_waitcnt lgkmcnt(0)
	s_nop 1
	v_mov_b32_dpp v5, v7 quad_perm:[2,3,0,1] row_mask:0xf bank_mask:0xf
	s_and_saveexec_b64 s[0:1], vcc
	s_cbranch_execz .LBB0_933


	v_med3_f32 v8, v8, s77, v166
	v_med3_f32 v7, v7, s77, v166

	v_cvt_pk_fp8_f32 v9, v8, v7

	s_waitcnt lgkmcnt(0)

	v_med3_f32 v6, v6, s77, v166
	v_med3_f32 v5, v5, s77, v166
	v_cvt_pk_fp8_f32 v9, v6, v5 op_sel:[0,0,1]
	global_store_dword v[2:3], v9, off offset:32
.LBB0_933:
	s_or_b64 exec, exec, s[0:1]
	v_mul_f32_e32 v8, v32, v4
	s_nop 1
	v_mov_b32_dpp v7, v8 quad_perm:[1,0,3,2] row_mask:0xf bank_mask:0xf
	s_nop 1
	v_mov_b32_dpp v6, v8 quad_perm:[2,3,0,1] row_mask:0xf bank_mask:0xf
	s_waitcnt lgkmcnt(0)
	s_nop 1
	v_mov_b32_dpp v5, v7 quad_perm:[2,3,0,1] row_mask:0xf bank_mask:0xf
	s_and_saveexec_b64 s[0:1], vcc
	s_cbranch_execz .LBB0_935


	v_med3_f32 v8, v8, s77, v166
	v_med3_f32 v7, v7, s77, v166

	v_cvt_pk_fp8_f32 v9, v8, v7

	s_waitcnt lgkmcnt(0)

	v_med3_f32 v6, v6, s77, v166
	v_med3_f32 v5, v5, s77, v166
	v_cvt_pk_fp8_f32 v9, v6, v5 op_sel:[0,0,1]
	global_store_dword v[2:3], v9, off offset:64
.LBB0_935:
	s_or_b64 exec, exec, s[0:1]
	v_mul_f32_e32 v7, v16, v4
	s_nop 1
	v_mov_b32_dpp v6, v7 quad_perm:[1,0,3,2] row_mask:0xf bank_mask:0xf
	s_waitcnt lgkmcnt(0)
	s_nop 1
	v_mov_b32_dpp v5, v7 quad_perm:[2,3,0,1] row_mask:0xf bank_mask:0xf
	s_nop 1
	v_mov_b32_dpp v4, v6 quad_perm:[2,3,0,1] row_mask:0xf bank_mask:0xf
	s_and_saveexec_b64 s[0:1], vcc
	s_cbranch_execz .LBB0_937


	v_med3_f32 v7, v7, s77, v166
	v_med3_f32 v6, v6, s77, v166

	v_cvt_pk_fp8_f32 v8, v7, v6
	s_waitcnt lgkmcnt(0)


	v_med3_f32 v5, v5, s77, v166
	v_med3_f32 v4, v4, s77, v166
	v_cvt_pk_fp8_f32 v8, v5, v4 op_sel:[0,0,1]
	global_store_dword v[2:3], v8, off offset:96
.LBB0_937:
	s_or_b64 exec, exec, s[0:1]
	ds_read_b32 v2, v72 offset:236
	s_waitcnt lgkmcnt(0)
	v_mul_f32_e32 v4, 0x41800000, v2
	v_mul_f32_e32 v8, v65, v4
	s_nop 1
	v_mov_b32_dpp v7, v8 quad_perm:[1,0,3,2] row_mask:0xf bank_mask:0xf
	s_nop 1
	v_mov_b32_dpp v6, v8 quad_perm:[2,3,0,1] row_mask:0xf bank_mask:0xf
	v_lshlrev_b64 v[2:3], 11, v[66:67]
	v_lshl_add_u64 v[2:3], v[68:69], 0, v[2:3]
	v_lshl_add_u64 v[2:3], v[2:3], 0, s[42:43]
	s_waitcnt lgkmcnt(0)
	s_nop 1
	v_mov_b32_dpp v5, v7 quad_perm:[2,3,0,1] row_mask:0xf bank_mask:0xf
	s_and_saveexec_b64 s[0:1], vcc
	s_cbranch_execz .LBB0_939


	v_med3_f32 v8, v8, s77, v166
	v_med3_f32 v7, v7, s77, v166

	v_cvt_pk_fp8_f32 v9, v8, v7

	s_waitcnt lgkmcnt(0)

	v_med3_f32 v6, v6, s77, v166
	v_med3_f32 v5, v5, s77, v166
	v_cvt_pk_fp8_f32 v9, v6, v5 op_sel:[0,0,1]
	global_store_dword v[2:3], v9, off
.LBB0_939:
	s_or_b64 exec, exec, s[0:1]
	v_mul_f32_e32 v8, v49, v4
	s_nop 1
	v_mov_b32_dpp v7, v8 quad_perm:[1,0,3,2] row_mask:0xf bank_mask:0xf
	s_nop 1
	v_mov_b32_dpp v6, v8 quad_perm:[2,3,0,1] row_mask:0xf bank_mask:0xf
	s_waitcnt lgkmcnt(0)
	s_nop 1
	v_mov_b32_dpp v5, v7 quad_perm:[2,3,0,1] row_mask:0xf bank_mask:0xf
	s_and_saveexec_b64 s[0:1], vcc
	s_cbranch_execz .LBB0_941


	v_med3_f32 v8, v8, s77, v166
	v_med3_f32 v7, v7, s77, v166

	v_cvt_pk_fp8_f32 v9, v8, v7

	s_waitcnt lgkmcnt(0)

	v_med3_f32 v6, v6, s77, v166
	v_med3_f32 v5, v5, s77, v166
	v_cvt_pk_fp8_f32 v9, v6, v5 op_sel:[0,0,1]
	global_store_dword v[2:3], v9, off offset:32
.LBB0_941:
	s_or_b64 exec, exec, s[0:1]
	v_mul_f32_e32 v8, v33, v4
	s_nop 1
	v_mov_b32_dpp v7, v8 quad_perm:[1,0,3,2] row_mask:0xf bank_mask:0xf
	s_nop 1
	v_mov_b32_dpp v6, v8 quad_perm:[2,3,0,1] row_mask:0xf bank_mask:0xf
	s_waitcnt lgkmcnt(0)
	s_nop 1
	v_mov_b32_dpp v5, v7 quad_perm:[2,3,0,1] row_mask:0xf bank_mask:0xf
	s_and_saveexec_b64 s[0:1], vcc
	s_cbranch_execz .LBB0_943


	v_med3_f32 v8, v8, s77, v166
	v_med3_f32 v7, v7, s77, v166

	v_cvt_pk_fp8_f32 v9, v8, v7

	s_waitcnt lgkmcnt(0)

	v_med3_f32 v6, v6, s77, v166
	v_med3_f32 v5, v5, s77, v166
	v_cvt_pk_fp8_f32 v9, v6, v5 op_sel:[0,0,1]
	global_store_dword v[2:3], v9, off offset:64
.LBB0_943:
	s_or_b64 exec, exec, s[0:1]
	v_mul_f32_e32 v7, v17, v4
	s_nop 1
	v_mov_b32_dpp v6, v7 quad_perm:[1,0,3,2] row_mask:0xf bank_mask:0xf
	s_waitcnt lgkmcnt(0)
	s_nop 1
	v_mov_b32_dpp v5, v7 quad_perm:[2,3,0,1] row_mask:0xf bank_mask:0xf
	s_nop 1
	v_mov_b32_dpp v4, v6 quad_perm:[2,3,0,1] row_mask:0xf bank_mask:0xf
	s_and_saveexec_b64 s[0:1], vcc
	s_cbranch_execz .LBB0_945


	v_med3_f32 v7, v7, s77, v166
	v_med3_f32 v6, v6, s77, v166

	v_cvt_pk_fp8_f32 v8, v7, v6
	s_waitcnt lgkmcnt(0)


	v_med3_f32 v5, v5, s77, v166
	v_med3_f32 v4, v4, s77, v166
	v_cvt_pk_fp8_f32 v8, v5, v4 op_sel:[0,0,1]
	global_store_dword v[2:3], v8, off offset:96

.LBB0_950:
	s_nop 7
	v_max_f32_e32 v177, v66, v67


	v_max3_f32 v177, v177, v68, v69
	v_max3_f32 v177, v177, v70, v71
	v_max3_f32 v177, v177, v72, v73
	v_max3_f32 v177, v177, v74, v75
	v_max3_f32 v177, v177, v76, v77
	v_max3_f32 v177, v177, v78, v79
	v_max3_f32 v177, v177, v80, v81
	v_max3_f32 v177, v177, v82, v83
	v_max3_f32 v177, v177, v84, v85
	v_max3_f32 v177, v177, v86, v87
	v_max3_f32 v177, v177, v88, v89
	v_max3_f32 v177, v177, v90, v91
	v_max3_f32 v177, v177, v92, v93
	v_max3_f32 v177, v177, v94, v95
	v_max3_f32 v177, v177, v96, v97
	v_mov_b32_e32 v178, v177
	s_nop 1
	v_permlane32_swap_b32_e32 v177, v178


	v_max_f32_e32 v177, v177, v178
	v_cmp_ge_f32_e32 vcc, s76, v177
	s_cmp_eq_u64 vcc, exec
	s_cbranch_scc0 .Lsm2_slow
	v_mov_b32_e32 v226, 1.0

.LBB0_958:
	s_or_b64 exec, exec, s[44:45]
	s_waitcnt lgkmcnt(0)
	s_lshl_b64 s[0:1], s[52:53], 11
	v_ashrrev_i32_e32 v73, 3, v170
	v_and_b32_e32 v66, -4, v73
	v_lshl_add_u32 v72, v66, 2, s65
	ds_read_b32 v67, v72 offset:128
	s_add_u32 s0, s61, s0
	s_addc_u32 s1, s62, s1
	s_add_u32 s0, s0, s79
	v_and_b32_e32 v148, 31, v170
	s_waitcnt lgkmcnt(0)
	v_mul_f32_e32 v74, 0x41800000, v67
	v_mul_f32_e32 v76, v50, v74
	s_nop 1
	v_mov_b32_dpp v75, v76 quad_perm:[1,0,3,2] row_mask:0xf bank_mask:0xf
	v_and_b32_e32 v50, 3, v170
	v_cmp_eq_u32_e32 vcc, 0, v50
	s_nop 1
	v_mov_b32_dpp v77, v76 quad_perm:[2,3,0,1] row_mask:0xf bank_mask:0xf
	s_addc_u32 s1, s1, 0
	s_waitcnt lgkmcnt(0)
	s_nop 1
	v_mov_b32_dpp v50, v75 quad_perm:[2,3,0,1] row_mask:0xf bank_mask:0xf
	v_ashrrev_i32_e32 v67, 31, v66
	v_lshl_add_u64 v[68:69], s[0:1], 0, v[148:149]
	v_lshlrev_b64 v[70:71], 11, v[66:67]
	v_lshl_add_u64 v[70:71], v[68:69], 0, v[70:71]
	s_and_saveexec_b64 s[0:1], vcc
	s_cbranch_execz .LBB0_960


	v_med3_f32 v76, v76, s77, v166
	v_med3_f32 v75, v75, s77, v166

	v_cvt_pk_fp8_f32 v78, v76, v75
	v_max_f32_e32 v77, v77, v77
	s_waitcnt lgkmcnt(0)

	v_med3_f32 v75, v77, s77, v166
	v_med3_f32 v50, v50, s77, v166
	v_cvt_pk_fp8_f32 v78, v75, v50 op_sel:[0,0,1]
	global_store_dword v[70:71], v78, off
.LBB0_960:
	s_or_b64 exec, exec, s[0:1]
	v_mul_f32_e32 v76, v34, v74
	s_nop 1
	v_mov_b32_dpp v75, v76 quad_perm:[1,0,3,2] row_mask:0xf bank_mask:0xf
	s_waitcnt lgkmcnt(0)
	s_nop 1
	v_mov_b32_dpp v50, v76 quad_perm:[2,3,0,1] row_mask:0xf bank_mask:0xf
	s_nop 1
	v_mov_b32_dpp v34, v75 quad_perm:[2,3,0,1] row_mask:0xf bank_mask:0xf
	s_and_saveexec_b64 s[0:1], vcc
	s_cbranch_execz .LBB0_962


	v_med3_f32 v76, v76, s77, v166
	v_med3_f32 v75, v75, s77, v166

	v_cvt_pk_fp8_f32 v77, v76, v75
	s_waitcnt lgkmcnt(0)


	v_med3_f32 v50, v50, s77, v166
	v_med3_f32 v34, v34, s77, v166
	v_cvt_pk_fp8_f32 v77, v50, v34 op_sel:[0,0,1]
	global_store_dword v[70:71], v77, off offset:32
.LBB0_962:
	s_or_b64 exec, exec, s[0:1]
	v_mul_f32_e32 v75, v18, v74
	s_waitcnt lgkmcnt(0)
	s_nop 1
	v_mov_b32_dpp v50, v75 quad_perm:[1,0,3,2] row_mask:0xf bank_mask:0xf
	s_nop 1
	v_mov_b32_dpp v34, v75 quad_perm:[2,3,0,1] row_mask:0xf bank_mask:0xf
	s_waitcnt lgkmcnt(0)
	s_nop 1
	v_mov_b32_dpp v18, v50 quad_perm:[2,3,0,1] row_mask:0xf bank_mask:0xf
	s_and_saveexec_b64 s[0:1], vcc
	s_cbranch_execz .LBB0_964


	v_med3_f32 v75, v75, s77, v166
	v_med3_f32 v50, v50, s77, v166

	v_cvt_pk_fp8_f32 v76, v75, v50

	s_waitcnt lgkmcnt(0)

	v_med3_f32 v34, v34, s77, v166
	v_med3_f32 v18, v18, s77, v166
	v_cvt_pk_fp8_f32 v76, v34, v18 op_sel:[0,0,1]
	global_store_dword v[70:71], v76, off offset:64
.LBB0_964:
	s_or_b64 exec, exec, s[0:1]
	v_mul_f32_e32 v50, v2, v74
	s_nop 1
	v_mov_b32_dpp v34, v50 quad_perm:[1,0,3,2] row_mask:0xf bank_mask:0xf
	s_waitcnt lgkmcnt(0)
	s_nop 1
	v_mov_b32_dpp v18, v50 quad_perm:[2,3,0,1] row_mask:0xf bank_mask:0xf
	s_nop 1
	v_mov_b32_dpp v2, v34 quad_perm:[2,3,0,1] row_mask:0xf bank_mask:0xf
	s_and_saveexec_b64 s[0:1], vcc
	s_cbranch_execz .LBB0_966


	v_med3_f32 v50, v50, s77, v166
	v_med3_f32 v34, v34, s77, v166

	v_cvt_pk_fp8_f32 v74, v50, v34
	s_waitcnt lgkmcnt(0)


	v_med3_f32 v18, v18, s77, v166
	v_med3_f32 v2, v2, s77, v166
	v_cvt_pk_fp8_f32 v74, v18, v2 op_sel:[0,0,1]
	global_store_dword v[70:71], v74, off offset:96
.LBB0_966:
	s_or_b64 exec, exec, s[0:1]
	s_waitcnt lgkmcnt(0)
	ds_read_b32 v2, v72 offset:132
	v_or_b32_e32 v50, 1, v66
	s_waitcnt lgkmcnt(0)
	v_mul_f32_e32 v2, 0x41800000, v2
	v_mul_f32_e32 v71, v51, v2
	s_nop 1
	v_mov_b32_dpp v70, v71 quad_perm:[1,0,3,2] row_mask:0xf bank_mask:0xf
	s_nop 1
	v_mov_b32_dpp v34, v71 quad_perm:[2,3,0,1] row_mask:0xf bank_mask:0xf
	v_ashrrev_i32_e32 v51, 31, v50
	v_lshlrev_b64 v[50:51], 11, v[50:51]
	v_lshl_add_u64 v[50:51], v[68:69], 0, v[50:51]
	s_waitcnt lgkmcnt(0)
	s_nop 1
	v_mov_b32_dpp v18, v70 quad_perm:[2,3,0,1] row_mask:0xf bank_mask:0xf
	s_and_saveexec_b64 s[0:1], vcc
	s_cbranch_execz .LBB0_968


	v_med3_f32 v71, v71, s77, v166
	v_med3_f32 v70, v70, s77, v166

	v_cvt_pk_fp8_f32 v74, v71, v70

	s_waitcnt lgkmcnt(0)

	v_med3_f32 v34, v34, s77, v166
	v_med3_f32 v18, v18, s77, v166
	v_cvt_pk_fp8_f32 v74, v34, v18 op_sel:[0,0,1]
	global_store_dword v[50:51], v74, off
.LBB0_968:
	s_or_b64 exec, exec, s[0:1]
	v_mul_f32_e32 v70, v35, v2
	s_nop 1
	v_mov_b32_dpp v35, v70 quad_perm:[1,0,3,2] row_mask:0xf bank_mask:0xf
	s_nop 1
	v_mov_b32_dpp v34, v70 quad_perm:[2,3,0,1] row_mask:0xf bank_mask:0xf
	s_waitcnt lgkmcnt(0)
	s_nop 1
	v_mov_b32_dpp v18, v35 quad_perm:[2,3,0,1] row_mask:0xf bank_mask:0xf
	s_and_saveexec_b64 s[0:1], vcc
	s_cbranch_execz .LBB0_970


	v_med3_f32 v70, v70, s77, v166
	v_med3_f32 v35, v35, s77, v166

	v_cvt_pk_fp8_f32 v71, v70, v35

	s_waitcnt lgkmcnt(0)

	v_med3_f32 v34, v34, s77, v166
	v_med3_f32 v18, v18, s77, v166
	v_cvt_pk_fp8_f32 v71, v34, v18 op_sel:[0,0,1]
	global_store_dword v[50:51], v71, off offset:32
.LBB0_970:
	s_or_b64 exec, exec, s[0:1]
	v_mul_f32_e32 v35, v19, v2
	s_nop 1
	v_mov_b32_dpp v34, v35 quad_perm:[1,0,3,2] row_mask:0xf bank_mask:0xf
	s_nop 1
	v_mov_b32_dpp v19, v35 quad_perm:[2,3,0,1] row_mask:0xf bank_mask:0xf
	s_waitcnt lgkmcnt(0)
	s_nop 1
	v_mov_b32_dpp v18, v34 quad_perm:[2,3,0,1] row_mask:0xf bank_mask:0xf
	s_and_saveexec_b64 s[0:1], vcc
	s_cbranch_execz .LBB0_972


	v_med3_f32 v35, v35, s77, v166
	v_med3_f32 v34, v34, s77, v166

	v_cvt_pk_fp8_f32 v70, v35, v34

	s_waitcnt lgkmcnt(0)

	v_med3_f32 v19, v19, s77, v166
	v_med3_f32 v18, v18, s77, v166
	v_cvt_pk_fp8_f32 v70, v19, v18 op_sel:[0,0,1]
	global_store_dword v[50:51], v70, off offset:64
.LBB0_972:
	s_or_b64 exec, exec, s[0:1]
	v_mul_f32_e32 v19, v3, v2
	s_waitcnt lgkmcnt(0)
	s_nop 1
	v_mov_b32_dpp v18, v19 quad_perm:[1,0,3,2] row_mask:0xf bank_mask:0xf
	s_nop 1
	v_mov_b32_dpp v3, v19 quad_perm:[2,3,0,1] row_mask:0xf bank_mask:0xf
	s_waitcnt lgkmcnt(0)
	s_nop 1
	v_mov_b32_dpp v2, v18 quad_perm:[2,3,0,1] row_mask:0xf bank_mask:0xf
	s_and_saveexec_b64 s[0:1], vcc
	s_cbranch_execz .LBB0_974


	v_med3_f32 v19, v19, s77, v166
	v_med3_f32 v18, v18, s77, v166

	v_cvt_pk_fp8_f32 v34, v19, v18

	s_waitcnt lgkmcnt(0)

	v_med3_f32 v3, v3, s77, v166
	v_med3_f32 v2, v2, s77, v166
	v_cvt_pk_fp8_f32 v34, v3, v2 op_sel:[0,0,1]
	global_store_dword v[50:51], v34, off offset:96
.LBB0_974:
	s_or_b64 exec, exec, s[0:1]
	s_waitcnt lgkmcnt(0)
	ds_read_b32 v2, v72 offset:136
	s_waitcnt lgkmcnt(0)
	v_mul_f32_e32 v18, 0x41800000, v2
	v_mul_f32_e32 v50, v52, v18
	s_nop 1
	v_mov_b32_dpp v35, v50 quad_perm:[1,0,3,2] row_mask:0xf bank_mask:0xf
	s_nop 1
	v_mov_b32_dpp v34, v50 quad_perm:[2,3,0,1] row_mask:0xf bank_mask:0xf
	v_or_b32_e32 v2, 2, v66
	v_ashrrev_i32_e32 v3, 31, v2
	v_lshlrev_b64 v[2:3], 11, v[2:3]
	s_waitcnt lgkmcnt(0)
	s_nop 1
	v_mov_b32_dpp v19, v35 quad_perm:[2,3,0,1] row_mask:0xf bank_mask:0xf
	v_lshl_add_u64 v[2:3], v[68:69], 0, v[2:3]
	s_and_saveexec_b64 s[0:1], vcc
	s_cbranch_execz .LBB0_976


	v_med3_f32 v50, v50, s77, v166
	v_med3_f32 v35, v35, s77, v166

	v_cvt_pk_fp8_f32 v51, v50, v35

	s_waitcnt lgkmcnt(0)

	v_med3_f32 v34, v34, s77, v166
	v_med3_f32 v19, v19, s77, v166
	v_cvt_pk_fp8_f32 v51, v34, v19 op_sel:[0,0,1]
	global_store_dword v[2:3], v51, off

.LBB0_1084:
	s_or_b64 exec, exec, s[0:1]
	v_mul_f32_e32 v7, v17, v4
	s_nop 1
	v_mov_b32_dpp v6, v7 quad_perm:[1,0,3,2] row_mask:0xf bank_mask:0xf
	s_waitcnt lgkmcnt(0)
	s_nop 1
	v_mov_b32_dpp v5, v7 quad_perm:[2,3,0,1] row_mask:0xf bank_mask:0xf
	s_nop 1
	v_mov_b32_dpp v4, v6 quad_perm:[2,3,0,1] row_mask:0xf bank_mask:0xf
	s_and_saveexec_b64 s[0:1], vcc
	s_cbranch_execz .LBB0_803


	v_med3_f32 v7, v7, s77, v166
	v_med3_f32 v6, v6, s77, v166

	v_cvt_pk_fp8_f32 v8, v7, v6
	s_waitcnt lgkmcnt(0)


	v_med3_f32 v5, v5, s77, v166
	v_med3_f32 v4, v4, s77, v166
	v_cvt_pk_fp8_f32 v8, v5, v4 op_sel:[0,0,1]
	global_store_dword v[2:3], v8, off offset:96
	s_branch .LBB0_803
